# baseline (speedup 1.0000x reference)
.LBB2_8:
	s_or_b64 exec, exec, s[2:3]
	v_and_b32_e32 v1, 56, v1
	v_or_b32_e32 v12, s8, v93
	s_lshl_b32 s2, s9, 1
	v_lshl_add_u32 v0, v1, 2, 0
	s_add_u32 s0, s0, s2
	v_mad_u64_u32 v[18:19], s[2:3], v12, s4, v[0:1]
	ds_read_b128 v[4:7], v18 offset:272
	ds_read_b128 v[8:11], v18 offset:288
	v_add_u32_e32 v20, s5, v12
	s_addc_u32 s1, s1, 0
	v_lshlrev_b32_e32 v2, 1, v1
	v_mov_b32_e32 v3, 0
	s_waitcnt lgkmcnt(0)
	v_cvt_pk_f16_f32 v11, v10, v11
	v_cvt_pk_f16_f32 v10, v8, v9
	v_cvt_pk_f16_f32 v9, v6, v7
	v_cvt_pk_f16_f32 v8, v4, v5
	ds_read_b128 v[4:7], v18 offset:2448
	ds_read_b128 v[12:15], v18 offset:2464
	v_ashrrev_i32_e32 v21, 31, v20
	v_lshl_add_u64 v[2:3], s[0:1], 0, v[2:3]
	v_lshlrev_b64 v[16:17], 10, v[20:21]
	v_lshl_add_u64 v[16:17], v[2:3], 0, v[16:17]
	global_store_dwordx4 v[16:17], v[8:11], off nt
	s_waitcnt lgkmcnt(1)
	v_cvt_pk_f16_f32 v7, v6, v7
	v_cvt_pk_f16_f32 v6, v4, v5
	s_waitcnt lgkmcnt(0)
	v_cvt_pk_f16_f32 v9, v14, v15
	v_cvt_pk_f16_f32 v8, v12, v13
	v_add_u32_e32 v4, 8, v20
	ds_read_b128 v[10:13], v18 offset:4624
	ds_read_b128 v[14:17], v18 offset:4640
	v_ashrrev_i32_e32 v5, 31, v4
	v_lshlrev_b64 v[4:5], 10, v[4:5]
	v_lshl_add_u64 v[4:5], v[2:3], 0, v[4:5]
	global_store_dwordx4 v[4:5], v[6:9], off nt
	s_waitcnt lgkmcnt(1)
	v_cvt_pk_f16_f32 v5, v12, v13
	v_cvt_pk_f16_f32 v4, v10, v11
	s_waitcnt lgkmcnt(0)
	v_cvt_pk_f16_f32 v7, v16, v17
	v_cvt_pk_f16_f32 v6, v14, v15
	v_add_u32_e32 v16, 16, v20
	ds_read_b128 v[8:11], v18 offset:6800
	ds_read_b128 v[12:15], v18 offset:6816
	v_ashrrev_i32_e32 v17, 31, v16
	v_lshlrev_b64 v[16:17], 10, v[16:17]
	v_lshl_add_u64 v[16:17], v[2:3], 0, v[16:17]
	global_store_dwordx4 v[16:17], v[4:7], off nt
	v_add_u32_e32 v16, 24, v20
	v_ashrrev_i32_e32 v17, 31, v16
	s_waitcnt lgkmcnt(0)
	v_cvt_pk_f16_f32 v7, v14, v15
	v_cvt_pk_f16_f32 v6, v12, v13
	v_cvt_pk_f16_f32 v5, v10, v11
	v_cvt_pk_f16_f32 v4, v8, v9
	ds_read_b128 v[8:11], v18 offset:8976
	ds_read_b128 v[12:15], v18 offset:8992
	v_lshlrev_b64 v[16:17], 10, v[16:17]
	v_lshl_add_u64 v[16:17], v[2:3], 0, v[16:17]
	global_store_dwordx4 v[16:17], v[4:7], off nt
	v_add_u32_e32 v16, 32, v20
	v_ashrrev_i32_e32 v17, 31, v16
	s_waitcnt lgkmcnt(0)
	v_cvt_pk_f16_f32 v7, v14, v15
	v_cvt_pk_f16_f32 v6, v12, v13
	v_cvt_pk_f16_f32 v5, v10, v11
	v_cvt_pk_f16_f32 v4, v8, v9
	ds_read_b128 v[8:11], v18 offset:11152
	ds_read_b128 v[12:15], v18 offset:11168
	v_lshlrev_b64 v[16:17], 10, v[16:17]
	v_lshl_add_u64 v[16:17], v[2:3], 0, v[16:17]
	global_store_dwordx4 v[16:17], v[4:7], off nt
	v_add_u32_e32 v16, 40, v20
	v_ashrrev_i32_e32 v17, 31, v16
	s_waitcnt lgkmcnt(0)
	v_cvt_pk_f16_f32 v7, v14, v15
	v_cvt_pk_f16_f32 v6, v12, v13
	v_cvt_pk_f16_f32 v5, v10, v11
	v_cvt_pk_f16_f32 v4, v8, v9
	ds_read_b128 v[8:11], v18 offset:13328
	ds_read_b128 v[12:15], v18 offset:13344
	v_lshlrev_b64 v[16:17], 10, v[16:17]
	v_lshl_add_u64 v[16:17], v[2:3], 0, v[16:17]
	global_store_dwordx4 v[16:17], v[4:7], off nt
	v_add_u32_e32 v16, 48, v20
	v_ashrrev_i32_e32 v17, 31, v16
	s_waitcnt lgkmcnt(0)
	v_cvt_pk_f16_f32 v7, v14, v15
	v_cvt_pk_f16_f32 v6, v12, v13
	v_cvt_pk_f16_f32 v5, v10, v11
	v_cvt_pk_f16_f32 v4, v8, v9
	ds_read_b128 v[8:11], v18 offset:15504
	ds_read_b128 v[12:15], v18 offset:15520
	v_lshlrev_b64 v[16:17], 10, v[16:17]
	v_lshl_add_u64 v[16:17], v[2:3], 0, v[16:17]
	global_store_dwordx4 v[16:17], v[4:7], off nt
	s_mul_i32 s0, s8, 0x110
	s_add_i32 s0, s0, 0
	s_waitcnt lgkmcnt(1)
	v_cvt_pk_f16_f32 v4, v8, v9
	v_add_u32_e32 v8, 56, v20
	v_ashrrev_i32_e32 v9, 31, v8
	v_lshlrev_b64 v[8:9], 10, v[8:9]
	v_lshlrev_b32_e32 v1, 2, v94
	s_waitcnt lgkmcnt(0)
	v_cvt_pk_f16_f32 v7, v14, v15
	v_cvt_pk_f16_f32 v6, v12, v13
	v_cvt_pk_f16_f32 v5, v10, v11
	v_lshl_add_u64 v[8:9], v[2:3], 0, v[8:9]
	v_add_u32_e32 v90, s0, v1
	global_store_dwordx4 v[8:9], v[4:7], off nt
	ds_read2_b32 v[4:5], v90 offset0:68 offset1:136
	v_add_u32_e32 v91, 0x200, v90
	ds_read2_b32 v[6:7], v91 offset0:76 offset1:144
	v_add_u32_e32 v92, 0x400, v90
	ds_read2_b32 v[8:9], v92 offset0:84 offset1:152
	v_add_u32_e32 v94, 0x600, v90
	s_waitcnt lgkmcnt(2)
	v_add_f32_e32 v68, 0, v4
	ds_read2_b32 v[10:11], v94 offset0:92 offset1:160
	v_add_f32_e32 v68, v68, v5
	v_add_u32_e32 v95, 0x800, v90
	s_waitcnt lgkmcnt(2)
	v_add_f32_e32 v68, v68, v6
	ds_read2_b32 v[12:13], v95 offset0:100 offset1:168
	v_add_f32_e32 v68, v68, v7
	v_add_u32_e32 v96, 0xa00, v90
	s_waitcnt lgkmcnt(2)
	v_add_f32_e32 v68, v68, v8
	ds_read2_b32 v[14:15], v96 offset0:108 offset1:176
	v_add_f32_e32 v68, v68, v9
	v_add_u32_e32 v97, 0xc00, v90
	s_waitcnt lgkmcnt(2)
	v_add_f32_e32 v68, v68, v10
	ds_read2_b32 v[16:17], v97 offset0:116 offset1:184
	v_add_f32_e32 v68, v68, v11
	v_add_u32_e32 v98, 0xe00, v90
	s_waitcnt lgkmcnt(2)
	v_add_f32_e32 v68, v68, v12
	ds_read2_b32 v[18:19], v98 offset0:124 offset1:192
	v_add_f32_e32 v68, v68, v13
	v_add_u32_e32 v99, 0x1000, v90
	s_waitcnt lgkmcnt(2)
	v_add_f32_e32 v68, v68, v14
	ds_read2_b32 v[20:21], v99 offset0:132 offset1:200
	v_add_f32_e32 v68, v68, v15
	s_waitcnt lgkmcnt(2)
	v_add_f32_e32 v68, v68, v16
	v_add_u32_e32 v100, 0x1400, v90
	v_add_f32_e32 v68, v68, v17
	ds_read2_b32 v[22:23], v100 offset0:12 offset1:80
	ds_read2_b32 v[24:25], v100 offset0:148 offset1:216
	s_waitcnt lgkmcnt(3)
	v_add_f32_e32 v68, v68, v18
	v_add_f32_e32 v68, v68, v19
	s_waitcnt lgkmcnt(2)
	v_add_f32_e32 v68, v68, v20
	v_add_u32_e32 v101, 0x1800, v90
	v_add_f32_e32 v68, v68, v21
	ds_read2_b32 v[26:27], v101 offset0:28 offset1:96
	ds_read2_b32 v[28:29], v101 offset0:164 offset1:232
	s_waitcnt lgkmcnt(3)
	v_add_f32_e32 v68, v68, v22
	v_add_f32_e32 v68, v68, v23
	s_waitcnt lgkmcnt(2)
	v_add_f32_e32 v68, v68, v24
	v_add_u32_e32 v102, 0x1c00, v90
	v_add_f32_e32 v68, v68, v25
	ds_read2_b32 v[30:31], v102 offset0:44 offset1:112
	ds_read2_b32 v[32:33], v102 offset0:180 offset1:248
	s_waitcnt lgkmcnt(3)
	v_add_f32_e32 v68, v68, v26
	v_add_f32_e32 v68, v68, v27
	v_add_u32_e32 v103, 0x2000, v90
	s_waitcnt lgkmcnt(2)
	v_add_f32_e32 v68, v68, v28
	ds_read2_b32 v[34:35], v103 offset0:60 offset1:128
	v_add_f32_e32 v68, v68, v29
	v_add_u32_e32 v104, 0x2200, v90
	s_waitcnt lgkmcnt(2)
	v_add_f32_e32 v68, v68, v30
	ds_read2_b32 v[36:37], v104 offset0:68 offset1:136
	v_add_f32_e32 v68, v68, v31
	v_add_u32_e32 v105, 0x2400, v90
	s_waitcnt lgkmcnt(2)
	v_add_f32_e32 v68, v68, v32
	ds_read2_b32 v[38:39], v105 offset0:76 offset1:144
	v_add_f32_e32 v68, v68, v33
	v_add_u32_e32 v106, 0x2600, v90
	s_waitcnt lgkmcnt(2)
	v_add_f32_e32 v68, v68, v34
	ds_read2_b32 v[40:41], v106 offset0:84 offset1:152
	v_add_f32_e32 v68, v68, v35
	v_add_u32_e32 v107, 0x2800, v90
	s_waitcnt lgkmcnt(2)
	v_add_f32_e32 v68, v68, v36
	ds_read2_b32 v[42:43], v107 offset0:92 offset1:160
	v_add_f32_e32 v68, v68, v37
	v_add_u32_e32 v108, 0x2a00, v90
	s_waitcnt lgkmcnt(2)
	v_add_f32_e32 v68, v68, v38
	ds_read2_b32 v[44:45], v108 offset0:100 offset1:168
	v_add_f32_e32 v68, v68, v39
	v_add_u32_e32 v109, 0x2c00, v90
	s_waitcnt lgkmcnt(2)
	v_add_f32_e32 v68, v68, v40
	ds_read2_b32 v[46:47], v109 offset0:108 offset1:176
	v_add_f32_e32 v68, v68, v41
	v_add_u32_e32 v110, 0x2e00, v90
	s_waitcnt lgkmcnt(2)
	v_add_f32_e32 v68, v68, v42
	ds_read2_b32 v[48:49], v110 offset0:116 offset1:184
	v_add_f32_e32 v68, v68, v43
	v_add_u32_e32 v111, 0x3000, v90
	s_waitcnt lgkmcnt(2)
	v_add_f32_e32 v68, v68, v44
	ds_read2_b32 v[50:51], v111 offset0:124 offset1:192
	v_add_f32_e32 v68, v68, v45
	s_waitcnt lgkmcnt(2)
	v_add_f32_e32 v68, v68, v46
	v_add_u32_e32 v112, 0x3400, v90
	v_add_f32_e32 v68, v68, v47
	ds_read2_b32 v[52:53], v112 offset0:4 offset1:72
	ds_read2_b32 v[54:55], v112 offset0:140 offset1:208
	s_waitcnt lgkmcnt(3)
	v_add_f32_e32 v68, v68, v48
	v_add_f32_e32 v68, v68, v49
	s_waitcnt lgkmcnt(2)
	v_add_f32_e32 v68, v68, v50
	v_add_u32_e32 v113, 0x3800, v90
	v_add_f32_e32 v68, v68, v51
	ds_read2_b32 v[56:57], v113 offset0:20 offset1:88
	ds_read2_b32 v[58:59], v113 offset0:156 offset1:224
	s_waitcnt lgkmcnt(3)
	v_add_f32_e32 v68, v68, v52
	v_add_f32_e32 v68, v68, v53
	s_waitcnt lgkmcnt(2)
	v_add_f32_e32 v68, v68, v54
	v_add_u32_e32 v114, 0x3c00, v90
	v_add_f32_e32 v68, v68, v55
	ds_read2_b32 v[60:61], v114 offset0:36 offset1:104
	ds_read2_b32 v[62:63], v114 offset0:172 offset1:240
	s_waitcnt lgkmcnt(3)
	v_add_f32_e32 v68, v68, v56
	v_add_f32_e32 v68, v68, v57
	v_add_u32_e32 v115, 0x4000, v90
	s_waitcnt lgkmcnt(2)
	v_add_f32_e32 v68, v68, v58
	ds_read2_b32 v[64:65], v115 offset0:52 offset1:120
	v_add_f32_e32 v68, v68, v59
	v_add_u32_e32 v116, 0x4200, v90
	s_waitcnt lgkmcnt(2)
	v_add_f32_e32 v68, v68, v60
	ds_read2_b32 v[66:67], v116 offset0:60 offset1:128
	v_add_f32_e32 v68, v68, v61
	s_waitcnt lgkmcnt(2)
	v_add_f32_e32 v68, v68, v62
	v_add_f32_e32 v68, v68, v63
	s_waitcnt lgkmcnt(1)
	v_add_f32_e32 v68, v68, v64
	v_add_f32_e32 v68, v68, v65
	s_lshl_b32 s0, s8, 2
	s_add_i32 s1, 0, 0x22110
	s_waitcnt lgkmcnt(0)
	v_add_f32_e32 v68, v68, v66
	s_add_i32 s0, s1, s0
	v_add_f32_e32 v68, v68, v67
	v_add_u32_e32 v69, s0, v1
	v_add_u32_e32 v1, s1, v1
	ds_write_b32 v69, v68
	s_waitcnt lgkmcnt(0)
	s_barrier
	ds_read2st64_b32 v[68:69], v1 offset1:1
	s_cmpk_gt_u32 s20, 0x7f
	v_cndmask_b32_e64 v117, 1.0, 0, s[6:7]
	ds_read2st64_b32 v[70:71], v1 offset0:2 offset1:3
	ds_read2st64_b32 v[88:89], v1 offset0:4 offset1:5
	ds_read_b32 v1, v1 offset:1536
	s_cselect_b64 s[0:1], -1, 0
	s_cmpk_gt_u32 s20, 0xbf
	s_waitcnt lgkmcnt(3)
	v_fma_f32 v68, v117, v68, 0
	v_cndmask_b32_e64 v117, 0, 1.0, s[0:1]
	s_cselect_b64 s[0:1], -1, 0
	s_cmpk_gt_u32 s20, 0xff
	v_fmac_f32_e32 v68, v117, v69
	v_cndmask_b32_e64 v69, 0, 1.0, s[0:1]
	s_cselect_b64 s[0:1], -1, 0
	s_cmpk_gt_u32 s20, 0x13f
	s_waitcnt lgkmcnt(2)
	v_fmac_f32_e32 v68, v69, v70
	v_cndmask_b32_e64 v69, 0, 1.0, s[0:1]
	s_cselect_b64 s[0:1], -1, 0
	s_cmpk_gt_u32 s20, 0x17f
	v_fmac_f32_e32 v68, v69, v71
	v_cndmask_b32_e64 v69, 0, 1.0, s[0:1]
	s_cselect_b64 s[0:1], -1, 0
	s_cmpk_gt_u32 s20, 0x1bf
	s_waitcnt lgkmcnt(1)
	v_fmac_f32_e32 v68, v69, v88
	v_cndmask_b32_e64 v69, 0, 1.0, s[0:1]
	s_cselect_b64 s[0:1], -1, 0
	v_fmac_f32_e32 v68, v69, v89
	v_cndmask_b32_e64 v69, 0, 1.0, s[0:1]
	s_waitcnt lgkmcnt(0)
	v_fmac_f32_e32 v68, v69, v1
	v_add_f32_e32 v1, v68, v4
	v_add_f32_e32 v4, v1, v5
	ds_write2_b32 v90, v1, v4 offset0:68 offset1:136
	v_add_f32_e32 v1, v4, v6
	v_add_f32_e32 v4, v1, v7
	ds_write2_b32 v91, v1, v4 offset0:76 offset1:144
	v_add_f32_e32 v1, v4, v8
	v_add_f32_e32 v4, v1, v9
	ds_write2_b32 v92, v1, v4 offset0:84 offset1:152
	v_add_f32_e32 v1, v4, v10
	v_add_f32_e32 v4, v1, v11
	ds_write2_b32 v94, v1, v4 offset0:92 offset1:160
	v_add_f32_e32 v1, v4, v12
	v_add_f32_e32 v4, v1, v13
	ds_write2_b32 v95, v1, v4 offset0:100 offset1:168
	v_add_f32_e32 v1, v4, v14
	v_add_f32_e32 v4, v1, v15
	ds_write2_b32 v96, v1, v4 offset0:108 offset1:176
	v_add_f32_e32 v1, v4, v16
	v_add_f32_e32 v4, v1, v17
	ds_write2_b32 v97, v1, v4 offset0:116 offset1:184
	v_add_f32_e32 v1, v4, v18
	v_add_f32_e32 v4, v1, v19
	ds_write2_b32 v98, v1, v4 offset0:124 offset1:192
	v_add_f32_e32 v1, v4, v20
	v_add_f32_e32 v4, v1, v21
	ds_write2_b32 v99, v1, v4 offset0:132 offset1:200
	v_add_f32_e32 v1, v4, v22
	v_add_f32_e32 v4, v1, v23
	ds_write2_b32 v100, v1, v4 offset0:12 offset1:80
	v_add_f32_e32 v1, v4, v24
	v_add_f32_e32 v4, v1, v25
	ds_write2_b32 v100, v1, v4 offset0:148 offset1:216
	v_add_f32_e32 v1, v4, v26
	v_add_f32_e32 v4, v1, v27
	ds_write2_b32 v101, v1, v4 offset0:28 offset1:96
	v_add_f32_e32 v1, v4, v28
	v_add_f32_e32 v4, v1, v29
	ds_write2_b32 v101, v1, v4 offset0:164 offset1:232
	v_add_f32_e32 v1, v4, v30
	v_add_f32_e32 v4, v1, v31
	ds_write2_b32 v102, v1, v4 offset0:44 offset1:112
	v_add_f32_e32 v1, v4, v32
	v_add_f32_e32 v4, v1, v33
	ds_write2_b32 v102, v1, v4 offset0:180 offset1:248
	v_add_f32_e32 v1, v4, v34
	v_add_f32_e32 v4, v1, v35
	ds_write2_b32 v103, v1, v4 offset0:60 offset1:128
	v_add_f32_e32 v1, v4, v36
	v_add_f32_e32 v4, v1, v37
	ds_write2_b32 v104, v1, v4 offset0:68 offset1:136
	v_add_f32_e32 v1, v4, v38
	v_add_f32_e32 v4, v1, v39
	ds_write2_b32 v105, v1, v4 offset0:76 offset1:144
	v_add_f32_e32 v1, v4, v40
	v_add_f32_e32 v4, v1, v41
	ds_write2_b32 v106, v1, v4 offset0:84 offset1:152
	v_add_f32_e32 v1, v4, v42
	v_add_f32_e32 v4, v1, v43
	ds_write2_b32 v107, v1, v4 offset0:92 offset1:160
	v_add_f32_e32 v1, v4, v44
	v_add_f32_e32 v4, v1, v45
	ds_write2_b32 v108, v1, v4 offset0:100 offset1:168
	v_add_f32_e32 v1, v4, v46
	v_add_f32_e32 v4, v1, v47
	ds_write2_b32 v109, v1, v4 offset0:108 offset1:176
	v_add_f32_e32 v1, v4, v48
	v_add_f32_e32 v4, v1, v49
	ds_write2_b32 v110, v1, v4 offset0:116 offset1:184
	v_add_f32_e32 v1, v4, v50
	v_add_f32_e32 v4, v1, v51
	ds_write2_b32 v111, v1, v4 offset0:124 offset1:192
	v_add_f32_e32 v1, v4, v52
	v_add_f32_e32 v4, v1, v53
	ds_write2_b32 v112, v1, v4 offset0:4 offset1:72
	v_add_f32_e32 v1, v4, v54
	v_add_f32_e32 v4, v1, v55
	ds_write2_b32 v112, v1, v4 offset0:140 offset1:208
	v_add_f32_e32 v1, v4, v56
	v_add_f32_e32 v4, v1, v57
	ds_write2_b32 v113, v1, v4 offset0:20 offset1:88
	v_add_f32_e32 v1, v4, v58
	v_add_f32_e32 v4, v1, v59
	ds_write2_b32 v113, v1, v4 offset0:156 offset1:224
	v_add_f32_e32 v1, v4, v60
	v_add_f32_e32 v4, v1, v61
	ds_write2_b32 v114, v1, v4 offset0:36 offset1:104
	v_add_f32_e32 v1, v4, v62
	v_add_f32_e32 v4, v1, v63
	ds_write2_b32 v114, v1, v4 offset0:172 offset1:240
	v_add_f32_e32 v1, v4, v64
	v_add_f32_e32 v4, v1, v65
	ds_write2_b32 v115, v1, v4 offset0:52 offset1:120
	v_add_f32_e32 v1, v4, v66
	v_add_f32_e32 v4, v1, v67
	ds_write2_b32 v116, v1, v4 offset0:60 offset1:128
	v_or_b32_e32 v1, s5, v93
	v_add_u32_e32 v4, s8, v1
	v_sub_u32_e32 v1, v87, v86
	v_mov_b32_e32 v25, 0x1ff
	v_mov_b32_e32 v26, 0x200
	v_cvt_f32_i32_e32 v1, v1
	v_med3_i32 v5, v86, 0, v25
	v_med3_i32 v10, v87, 1, v26
	v_mad_u32_u24 v5, v5, s4, v0
	v_mad_u32_u24 v18, v10, s4, v0
	s_waitcnt lgkmcnt(0)
	s_barrier
	ds_read_b128 v[6:9], v5
	ds_read_b128 v[10:13], v18
	ds_read_b128 v[14:17], v5 offset:16
	ds_read_b128 v[18:21], v18 offset:16
	v_rcp_iflag_f32_e32 v22, v1
	s_mov_b64 s[0:1], 0x1000000
	v_ashrrev_i32_e32 v5, 31, v4
	s_waitcnt lgkmcnt(2)
	v_sub_f32_e32 v7, v11, v7
	v_sub_f32_e32 v6, v10, v6
	v_sub_f32_e32 v9, v13, v9
	v_sub_f32_e32 v8, v12, v8
	v_pk_mul_f32 v[10:11], v[8:9], v[22:23] op_sel_hi:[1,0]
	v_pk_mul_f32 v[12:13], v[6:7], v[22:23] op_sel_hi:[1,0]
	s_waitcnt lgkmcnt(0)
	v_sub_f32_e32 v7, v19, v15
	v_sub_f32_e32 v6, v18, v14
	v_sub_f32_e32 v9, v21, v17
	v_sub_f32_e32 v8, v20, v16
	v_pk_mul_f32 v[8:9], v[8:9], v[22:23] op_sel_hi:[1,0]
	v_pk_mul_f32 v[6:7], v[6:7], v[22:23] op_sel_hi:[1,0]
	v_lshl_add_u64 v[2:3], v[2:3], 0, s[0:1]
	v_cvt_pk_f16_f32 v9, v8, v9
	v_cvt_pk_f16_f32 v8, v6, v7
	v_cvt_pk_f16_f32 v7, v10, v11
	v_lshlrev_b64 v[10:11], 10, v[4:5]
	v_cvt_pk_f16_f32 v6, v12, v13
	v_lshl_add_u64 v[10:11], v[2:3], 0, v[10:11]
	v_sub_u32_e32 v1, v85, v84
	global_store_dwordx4 v[10:11], v[6:9], off
	v_cvt_f32_i32_e32 v1, v1
	v_med3_i32 v5, v84, 0, v25
	v_med3_i32 v10, v85, 1, v26
	v_mad_u32_u24 v5, v5, s4, v0
	v_mad_u32_u24 v18, v10, s4, v0
	ds_read_b128 v[6:9], v5
	ds_read_b128 v[10:13], v18
	ds_read_b128 v[14:17], v5 offset:16
	ds_read_b128 v[18:21], v18 offset:16
	v_rcp_iflag_f32_e32 v24, v1
	v_or_b32_e32 v22, 8, v4
	v_ashrrev_i32_e32 v23, 31, v22
	s_waitcnt lgkmcnt(2)
	v_sub_f32_e32 v7, v11, v7
	v_sub_f32_e32 v6, v10, v6
	v_sub_f32_e32 v9, v13, v9
	v_sub_f32_e32 v8, v12, v8
	v_pk_mul_f32 v[10:11], v[8:9], v[24:25] op_sel_hi:[1,0]
	v_pk_mul_f32 v[12:13], v[6:7], v[24:25] op_sel_hi:[1,0]
	s_waitcnt lgkmcnt(0)
	v_sub_f32_e32 v7, v19, v15
	v_sub_f32_e32 v6, v18, v14
	v_sub_f32_e32 v9, v21, v17
	v_sub_f32_e32 v8, v20, v16
	v_pk_mul_f32 v[8:9], v[8:9], v[24:25] op_sel_hi:[1,0]
	v_pk_mul_f32 v[6:7], v[6:7], v[24:25] op_sel_hi:[1,0]
	v_cvt_pk_f16_f32 v9, v8, v9
	v_cvt_pk_f16_f32 v8, v6, v7
	v_cvt_pk_f16_f32 v7, v10, v11
	v_lshlrev_b64 v[10:11], 10, v[22:23]
	v_cvt_pk_f16_f32 v6, v12, v13
	v_lshl_add_u64 v[10:11], v[2:3], 0, v[10:11]
	v_sub_u32_e32 v1, v83, v82
	global_store_dwordx4 v[10:11], v[6:9], off
	v_cvt_f32_i32_e32 v1, v1
	v_med3_i32 v5, v82, 0, v25
	v_med3_i32 v10, v83, 1, v26
	v_mad_u32_u24 v5, v5, s4, v0
	v_mad_u32_u24 v18, v10, s4, v0
	ds_read_b128 v[6:9], v5
	ds_read_b128 v[10:13], v18
	ds_read_b128 v[14:17], v5 offset:16
	ds_read_b128 v[18:21], v18 offset:16
	v_rcp_iflag_f32_e32 v24, v1
	v_or_b32_e32 v22, 16, v4
	v_ashrrev_i32_e32 v23, 31, v22
	s_waitcnt lgkmcnt(2)
	v_sub_f32_e32 v7, v11, v7
	v_sub_f32_e32 v6, v10, v6
	v_sub_f32_e32 v9, v13, v9
	v_sub_f32_e32 v8, v12, v8
	v_pk_mul_f32 v[10:11], v[8:9], v[24:25] op_sel_hi:[1,0]
	v_pk_mul_f32 v[12:13], v[6:7], v[24:25] op_sel_hi:[1,0]
	s_waitcnt lgkmcnt(0)
	v_sub_f32_e32 v7, v19, v15
	v_sub_f32_e32 v6, v18, v14
	v_sub_f32_e32 v9, v21, v17
	v_sub_f32_e32 v8, v20, v16
	v_pk_mul_f32 v[8:9], v[8:9], v[24:25] op_sel_hi:[1,0]
	v_pk_mul_f32 v[6:7], v[6:7], v[24:25] op_sel_hi:[1,0]
	v_cvt_pk_f16_f32 v9, v8, v9
	v_cvt_pk_f16_f32 v8, v6, v7
	v_cvt_pk_f16_f32 v7, v10, v11
	v_lshlrev_b64 v[10:11], 10, v[22:23]
	v_cvt_pk_f16_f32 v6, v12, v13
	v_lshl_add_u64 v[10:11], v[2:3], 0, v[10:11]
	v_sub_u32_e32 v1, v81, v80
	global_store_dwordx4 v[10:11], v[6:9], off
	v_cvt_f32_i32_e32 v1, v1
	v_med3_i32 v5, v80, 0, v25
	v_med3_i32 v10, v81, 1, v26
	v_mad_u32_u24 v5, v5, s4, v0
	v_mad_u32_u24 v18, v10, s4, v0
	ds_read_b128 v[6:9], v5
	ds_read_b128 v[10:13], v18
	ds_read_b128 v[14:17], v5 offset:16
	ds_read_b128 v[18:21], v18 offset:16
	v_rcp_iflag_f32_e32 v24, v1
	v_or_b32_e32 v22, 24, v4
	v_ashrrev_i32_e32 v23, 31, v22
	s_waitcnt lgkmcnt(2)
	v_sub_f32_e32 v7, v11, v7
	v_sub_f32_e32 v6, v10, v6
	v_sub_f32_e32 v9, v13, v9
	v_sub_f32_e32 v8, v12, v8
	v_pk_mul_f32 v[10:11], v[8:9], v[24:25] op_sel_hi:[1,0]
	v_pk_mul_f32 v[12:13], v[6:7], v[24:25] op_sel_hi:[1,0]
	s_waitcnt lgkmcnt(0)
	v_sub_f32_e32 v7, v19, v15
	v_sub_f32_e32 v6, v18, v14
	v_sub_f32_e32 v9, v21, v17
	v_sub_f32_e32 v8, v20, v16
	v_pk_mul_f32 v[8:9], v[8:9], v[24:25] op_sel_hi:[1,0]
	v_pk_mul_f32 v[6:7], v[6:7], v[24:25] op_sel_hi:[1,0]
	v_cvt_pk_f16_f32 v9, v8, v9
	v_cvt_pk_f16_f32 v8, v6, v7
	v_cvt_pk_f16_f32 v7, v10, v11
	v_lshlrev_b64 v[10:11], 10, v[22:23]
	v_cvt_pk_f16_f32 v6, v12, v13
	v_lshl_add_u64 v[10:11], v[2:3], 0, v[10:11]
	v_sub_u32_e32 v1, v79, v78
	global_store_dwordx4 v[10:11], v[6:9], off
	v_cvt_f32_i32_e32 v1, v1
	v_med3_i32 v5, v78, 0, v25
	v_med3_i32 v10, v79, 1, v26
	v_mad_u32_u24 v5, v5, s4, v0
	v_mad_u32_u24 v18, v10, s4, v0
	ds_read_b128 v[6:9], v5
	ds_read_b128 v[10:13], v18
	ds_read_b128 v[14:17], v5 offset:16
	ds_read_b128 v[18:21], v18 offset:16
	v_rcp_iflag_f32_e32 v24, v1
	v_or_b32_e32 v22, 32, v4
	v_ashrrev_i32_e32 v23, 31, v22
	s_waitcnt lgkmcnt(2)
	v_sub_f32_e32 v7, v11, v7
	v_sub_f32_e32 v6, v10, v6
	v_sub_f32_e32 v9, v13, v9
	v_sub_f32_e32 v8, v12, v8
	v_pk_mul_f32 v[10:11], v[8:9], v[24:25] op_sel_hi:[1,0]
	v_pk_mul_f32 v[12:13], v[6:7], v[24:25] op_sel_hi:[1,0]
	s_waitcnt lgkmcnt(0)
	v_sub_f32_e32 v7, v19, v15
	v_sub_f32_e32 v6, v18, v14
	v_sub_f32_e32 v9, v21, v17
	v_sub_f32_e32 v8, v20, v16
	v_pk_mul_f32 v[8:9], v[8:9], v[24:25] op_sel_hi:[1,0]
	v_pk_mul_f32 v[6:7], v[6:7], v[24:25] op_sel_hi:[1,0]
	v_cvt_pk_f16_f32 v9, v8, v9
	v_cvt_pk_f16_f32 v8, v6, v7
	v_cvt_pk_f16_f32 v7, v10, v11
	v_lshlrev_b64 v[10:11], 10, v[22:23]
	v_cvt_pk_f16_f32 v6, v12, v13
	v_lshl_add_u64 v[10:11], v[2:3], 0, v[10:11]
	v_sub_u32_e32 v1, v77, v76
	global_store_dwordx4 v[10:11], v[6:9], off
	v_cvt_f32_i32_e32 v1, v1
	v_med3_i32 v5, v76, 0, v25
	v_med3_i32 v10, v77, 1, v26
	v_mad_u32_u24 v5, v5, s4, v0
	v_mad_u32_u24 v18, v10, s4, v0
	ds_read_b128 v[6:9], v5
	ds_read_b128 v[10:13], v18
	ds_read_b128 v[14:17], v5 offset:16
	ds_read_b128 v[18:21], v18 offset:16
	v_rcp_iflag_f32_e32 v24, v1
	v_or_b32_e32 v22, 40, v4
	v_ashrrev_i32_e32 v23, 31, v22
	s_waitcnt lgkmcnt(2)
	v_sub_f32_e32 v7, v11, v7
	v_sub_f32_e32 v6, v10, v6
	v_sub_f32_e32 v9, v13, v9
	v_sub_f32_e32 v8, v12, v8
	v_pk_mul_f32 v[10:11], v[8:9], v[24:25] op_sel_hi:[1,0]
	v_pk_mul_f32 v[12:13], v[6:7], v[24:25] op_sel_hi:[1,0]
	s_waitcnt lgkmcnt(0)
	v_sub_f32_e32 v7, v19, v15
	v_sub_f32_e32 v6, v18, v14
	v_sub_f32_e32 v9, v21, v17
	v_sub_f32_e32 v8, v20, v16
	v_pk_mul_f32 v[8:9], v[8:9], v[24:25] op_sel_hi:[1,0]
	v_pk_mul_f32 v[6:7], v[6:7], v[24:25] op_sel_hi:[1,0]
	v_cvt_pk_f16_f32 v9, v8, v9
	v_cvt_pk_f16_f32 v8, v6, v7
	v_cvt_pk_f16_f32 v7, v10, v11
	v_lshlrev_b64 v[10:11], 10, v[22:23]
	v_cvt_pk_f16_f32 v6, v12, v13
	v_lshl_add_u64 v[10:11], v[2:3], 0, v[10:11]
	v_sub_u32_e32 v1, v75, v74
	global_store_dwordx4 v[10:11], v[6:9], off
	v_cvt_f32_i32_e32 v1, v1
	v_med3_i32 v5, v74, 0, v25
	v_med3_i32 v10, v75, 1, v26
	v_mad_u32_u24 v5, v5, s4, v0
	v_mad_u32_u24 v18, v10, s4, v0
	ds_read_b128 v[6:9], v5
	ds_read_b128 v[10:13], v18
	ds_read_b128 v[14:17], v5 offset:16
	ds_read_b128 v[18:21], v18 offset:16
	v_rcp_iflag_f32_e32 v24, v1
	v_or_b32_e32 v22, 48, v4
	v_ashrrev_i32_e32 v23, 31, v22
	s_waitcnt lgkmcnt(2)
	v_sub_f32_e32 v7, v11, v7
	v_sub_f32_e32 v6, v10, v6
	v_sub_f32_e32 v9, v13, v9
	v_sub_f32_e32 v8, v12, v8
	v_pk_mul_f32 v[10:11], v[8:9], v[24:25] op_sel_hi:[1,0]
	v_pk_mul_f32 v[12:13], v[6:7], v[24:25] op_sel_hi:[1,0]
	s_waitcnt lgkmcnt(0)
	v_sub_f32_e32 v7, v19, v15
	v_sub_f32_e32 v6, v18, v14
	v_sub_f32_e32 v9, v21, v17
	v_sub_f32_e32 v8, v20, v16
	v_pk_mul_f32 v[8:9], v[8:9], v[24:25] op_sel_hi:[1,0]
	v_pk_mul_f32 v[6:7], v[6:7], v[24:25] op_sel_hi:[1,0]
	v_cvt_pk_f16_f32 v9, v8, v9
	v_cvt_pk_f16_f32 v8, v6, v7
	v_cvt_pk_f16_f32 v7, v10, v11
	v_lshlrev_b64 v[10:11], 10, v[22:23]
	v_cvt_pk_f16_f32 v6, v12, v13
	v_lshl_add_u64 v[10:11], v[2:3], 0, v[10:11]
	v_sub_u32_e32 v1, v73, v72
	global_store_dwordx4 v[10:11], v[6:9], off
	v_cvt_f32_i32_e32 v1, v1
	v_med3_i32 v5, v72, 0, v25
	v_med3_i32 v10, v73, 1, v26
	v_mad_u32_u24 v5, v5, s4, v0
	v_mad_u32_u24 v18, v10, s4, v0
	ds_read_b128 v[6:9], v5
	ds_read_b128 v[10:13], v18
	ds_read_b128 v[14:17], v5 offset:16
	ds_read_b128 v[18:21], v18 offset:16
	v_or_b32_e32 v0, 56, v4
	v_rcp_iflag_f32_e32 v4, v1
	v_ashrrev_i32_e32 v1, 31, v0
	s_waitcnt lgkmcnt(2)
	v_sub_f32_e32 v7, v11, v7
	v_sub_f32_e32 v6, v10, v6
	v_sub_f32_e32 v9, v13, v9
	v_sub_f32_e32 v8, v12, v8
	v_pk_mul_f32 v[10:11], v[6:7], v[4:5] op_sel_hi:[1,0]
	s_waitcnt lgkmcnt(0)
	v_sub_f32_e32 v7, v19, v15
	v_sub_f32_e32 v6, v18, v14
	v_sub_f32_e32 v13, v21, v17
	v_sub_f32_e32 v12, v20, v16
	v_pk_mul_f32 v[8:9], v[8:9], v[4:5] op_sel_hi:[1,0]
	v_pk_mul_f32 v[12:13], v[12:13], v[4:5] op_sel_hi:[1,0]
	v_pk_mul_f32 v[4:5], v[6:7], v[4:5] op_sel_hi:[1,0]
	v_lshlrev_b64 v[0:1], 10, v[0:1]
	v_cvt_pk_f16_f32 v7, v12, v13
	v_cvt_pk_f16_f32 v6, v4, v5
	v_cvt_pk_f16_f32 v5, v8, v9
	v_cvt_pk_f16_f32 v4, v10, v11
	v_lshl_add_u64 v[0:1], v[2:3], 0, v[0:1]
	global_store_dwordx4 v[0:1], v[4:7], off
	s_endpgm
	.p2align	8
